# MLA steady loop of waves 0-3: MFMA-first after the barrier, the three LDS-DMA issues placed behind QK MFMAs 1-3
# baseline (speedup 1.0000x reference)
; #define SFENCE() __builtin_amdgcn_sched_barrier(0)
; template <bool FOX>
; __device__ __forceinline__ void attn_unit(const Args& A, int b, int h, int qb, LAS char* shm, LAS float* dg) {
;     ...
;           const lds_cptr vp = vp0 + ((t - 1) % NS) * VSLOT; float sa = 0.f, sb = 0.f;
; #pragma unroll
;           for (int g = 0; g < 2 * NQ; ++g) {
;               if (!FOX && g == 0) c0 = __builtin_amdgcn_mfma_f32_32x32x16_bf16(kf[0], qr[0], negm, 0, 0, 0);
;               else if (!FOX && g == 1) c1 = __builtin_amdgcn_mfma_f32_32x32x16_bf16(kf[1], qr[0], negm, 0, 0, 0);
;               else if (g & 1) c1 = __builtin_amdgcn_mfma_f32_32x32x16_bf16(kf[g], qr[g >> 1], c1, 0, 0, 0); else c0 = __builtin_amdgcn_mfma_f32_32x32x16_bf16(kf[g], qr[g >> 1], c0, 0, 0, 0);
;               if (g < 8) { const int i = (g >> 1) + 4 * (g & 1); vlo[i] = vtr(vp + (i >> 2) * 4096 + (i & 3) * 1024); vhi[i] = vtr(vp + (i >> 2) * 4096 + (i & 3) * 1024 + 512);
;                   if (g < 4) { sa += pp0[4 * g]; sb += pp0[4 * g + 1]; sa += pp0[4 * g + 2]; sb += pp0[4 * g + 3]; } else { sa += pp1[4 * g - 16]; sb += pp1[4 * g - 15]; sa += pp1[4 * g - 14]; sb += pp1[4 * g - 13]; }
;                   asm volatile("" : "+v"(sa), "+v"(sb)); }
;               { constexpr int G0 = FOX ? 0 : 4; if (g >= G0) { const int q = 2 * (g - G0);
; #pragma unroll
;                   for (int k = 0; k < 2; ++k) { const int w = q + k; const unsigned pkd = w < 8 ? cvt_pk_bf16(pp0[2 * w], pp0[2 * w + 1]) : cvt_pk_bf16(pp1[2 * w - 16], pp1[2 * w - 15]); pw[w >> 2][w & 3] = pkd; } } }
;               SFENCE();
;           }
;           lrun += sa + sb; }
;         MASKONLY(t);
;         float rm; ROWMAX(rm);
;         bool resc = false;
;         if (__any(rm > THR)) { const float dl = fmaxf(rm, 0.f); mhat += dl;
; #pragma unroll
;             for (int r = 0; r < 16; ++r) { c0[r] -= dl; c1[r] -= dl; }
;             if constexpr (!FOX) {
; #pragma unroll
;                 for (int r = 0; r < 16; ++r) negm[r] = -mhat;
;                 asm volatile("" : "+v"(negm)); }
;             const float f = __builtin_amdgcn_exp2f(-dl); lrun *= f; if (hi == 0) wsf[r32] = f; resc = true; }
;         SFENCE();
;         { const lds_cptr kp = kp0 + ((t + 1) % NS) * KSLOT;
; #pragma unroll
;           for (int g = 0; g < 8; ++g) { const int i = (g >> 1) + 4 * (g & 1);
.Lmla_ss1_in:
	s_mov_b32 m0, s52
	s_waitcnt lgkmcnt(0)
	s_add_i32 s27, s42, 0x8000
	v_mfma_f32_32x32x16_bf16 v[114:129], v[206:209], v[138:141], v[82:97]
	global_load_lds_dwordx4 v[234:235], off
	s_add_i32 m0, s52, 0x2000
	s_and_b32 s27, s27, 0x6000
	s_add_u32 s42, s42, 0x2000
	s_addc_u32 s43, s43, 0
	v_add_u32_e32 v3, s27, v247
	ds_read_b64_tr_b16 v[206:207], v3 offset:49152
	ds_read_b64_tr_b16 v[208:209], v3 offset:49664
	v_add_f32_e32 v4, 0, v67
	v_add_f32_e32 v5, 0, v66
	v_add_f32_e32 v4, v69, v4
	v_add_f32_e32 v5, v68, v5
	v_mfma_f32_32x32x16_bf16 v[98:113], v[194:197], v[138:141], v[82:97]
	global_load_lds_dwordx4 v[240:241], off
	s_mov_b32 m0, s53
	ds_read_b64_tr_b16 v[194:195], v3 offset:53248
	ds_read_b64_tr_b16 v[196:197], v3 offset:53760
	v_add_f32_e32 v4, v71, v4
	v_add_f32_e32 v5, v70, v5
	v_add_f32_e32 v4, v73, v4
	v_add_f32_e32 v5, v72, v5
	v_mfma_f32_32x32x16_bf16 v[114:129], v[202:205], v[142:145], v[114:129]
	global_load_lds_dwordx4 v[250:251], off
	ds_read_b64_tr_b16 v[202:203], v3 offset:50176
	ds_read_b64_tr_b16 v[204:205], v3 offset:50688
	v_add_f32_e32 v4, v75, v4
	v_add_f32_e32 v5, v74, v5
	v_add_f32_e32 v4, v77, v4
	v_add_f32_e32 v5, v76, v5
	v_mfma_f32_32x32x16_bf16 v[98:113], v[186:189], v[142:145], v[98:113]
	ds_read_b64_tr_b16 v[214:215], v3 offset:54272
	ds_read_b64_tr_b16 v[216:217], v3 offset:54784
	v_add_f32_e32 v4, v79, v4
	v_add_f32_e32 v5, v78, v5
	v_add_f32_e32 v4, v81, v4
	v_add_f32_e32 v5, v80, v5
	v_mfma_f32_32x32x16_bf16 v[114:129], v[198:201], v[146:149], v[114:129]
	ds_read_b64_tr_b16 v[210:211], v3 offset:51200
	ds_read_b64_tr_b16 v[212:213], v3 offset:51712
	v_add_f32_e32 v4, v51, v4
	v_add_f32_e32 v5, v50, v5
	v_add_f32_e32 v4, v53, v4
	v_add_f32_e32 v5, v52, v5
	v_mfma_f32_32x32x16_bf16 v[98:113], v[182:185], v[146:149], v[98:113]
	ds_read_b64_tr_b16 v[12:13], v3 offset:55296
	ds_read_b64_tr_b16 v[14:15], v3 offset:55808
	v_add_f32_e32 v4, v55, v4
	v_add_f32_e32 v5, v54, v5
	v_add_f32_e32 v4, v57, v4
	v_add_f32_e32 v5, v56, v5
	v_mfma_f32_32x32x16_bf16 v[114:129], v[190:193], v[150:153], v[114:129]
	ds_read_b64_tr_b16 v[8:9], v3 offset:52224
	ds_read_b64_tr_b16 v[10:11], v3 offset:52736
	v_add_f32_e32 v4, v59, v4
	v_add_f32_e32 v16, v61, v4
	v_add_f32_e32 v4, v58, v5
	v_add_f32_e32 v17, v60, v4
	v_mfma_f32_32x32x16_bf16 v[98:113], v[170:173], v[150:153], v[98:113]
	v_lshl_add_u64 v[234:235], v[234:235], 0, s[62:63]
	s_and_b32 s64, s26, 3
	ds_read_b64_tr_b16 v[4:5], v3 offset:56320
	ds_read_b64_tr_b16 v[6:7], v3 offset:56832
	v_add_f32_e32 v3, v63, v16
	v_add_f32_e32 v16, v62, v17
	v_add_f32_e32 v3, v65, v3
	v_add_f32_e32 v16, v64, v16
	v_mfma_f32_32x32x16_bf16 v[114:129], v[178:181], v[154:157], v[114:129]
	s_mulk_i32 s64, 0x3000
	v_lshl_add_u64 v[250:251], v[232:233], 0, s[42:43]
	v_cvt_pk_bf16_f32 v178, v50, v51
	v_cvt_pk_bf16_f32 v179, v52, v53
	v_cvt_pk_bf16_f32 v186, v66, v67
	v_cvt_pk_bf16_f32 v187, v68, v69
	v_mfma_f32_32x32x16_bf16 v[98:113], v[166:169], v[154:157], v[98:113]
	s_add_i32 s52, s64, s91
	s_add_i32 s64, s42, 0x6000
	v_lshl_add_u64 v[240:241], v[234:235], 0, s[56:57]
	v_cvt_pk_bf16_f32 v180, v54, v55
	v_cvt_pk_bf16_f32 v181, v56, v57
	v_cvt_pk_bf16_f32 v188, v70, v71
	v_cvt_pk_bf16_f32 v189, v72, v73
	v_mfma_f32_32x32x16_bf16 v[114:129], v[174:177], v[158:161], v[114:129]
	s_and_b32 s64, s64, 0x6000
	s_add_i32 s53, s64, s93
	v_cvt_pk_bf16_f32 v218, v58, v59
	v_cvt_pk_bf16_f32 v219, v60, v61
	v_cvt_pk_bf16_f32 v182, v74, v75
	v_cvt_pk_bf16_f32 v183, v76, v77
	v_mfma_f32_32x32x16_bf16 v[98:113], v[162:165], v[158:161], v[98:113]
	v_cvt_pk_bf16_f32 v220, v62, v63
	v_cvt_pk_bf16_f32 v221, v64, v65
	v_cvt_pk_bf16_f32 v184, v78, v79
	v_cvt_pk_bf16_f32 v185, v80, v81
	v_add_f32_e32 v3, v3, v16
	v_add_f32_e32 v246, v246, v3
	s_nop 3
	s_waitcnt lgkmcnt(0)
	v_mfma_f32_32x32x16_bf16 v[18:33], v[186:189], v[206:209], v[18:33]
	s_add_i32 s27, s26, 1
	s_and_b32 s64, s27, 3
	s_mulk_i32 s64, 0x3000
	v_exp_f32_e32 v66, v114
	v_exp_f32_e32 v67, v115
	v_exp_f32_e32 v68, v116
	v_exp_f32_e32 v69, v117
	v_add_u32_e32 v3, s64, v248
	v_mfma_f32_32x32x16_bf16 v[34:49], v[186:189], v[194:197], v[34:49]
	v_exp_f32_e32 v70, v118
	v_exp_f32_e32 v71, v119
	v_exp_f32_e32 v72, v120
	v_exp_f32_e32 v73, v121
	ds_read_b128 v[206:209], v3
	ds_read_b128 v[194:197], v3 offset:512
	v_mfma_f32_32x32x16_bf16 v[18:33], v[182:185], v[202:205], v[18:33]
	v_exp_f32_e32 v74, v122
	v_exp_f32_e32 v75, v123
	v_exp_f32_e32 v76, v124
	v_exp_f32_e32 v77, v125
	ds_read_b128 v[202:205], v3 offset:2048
	ds_read_b128 v[186:189], v3 offset:2560
	v_mfma_f32_32x32x16_bf16 v[34:49], v[182:185], v[214:217], v[34:49]
	v_exp_f32_e32 v78, v126
	v_exp_f32_e32 v79, v127
	v_exp_f32_e32 v80, v128
	v_exp_f32_e32 v81, v129
	ds_read_b128 v[198:201], v3 offset:4096
	ds_read_b128 v[182:185], v3 offset:4608
	v_mfma_f32_32x32x16_bf16 v[18:33], v[178:181], v[210:213], v[18:33]
	v_exp_f32_e32 v50, v98
	v_exp_f32_e32 v51, v99
	v_exp_f32_e32 v52, v100
	v_exp_f32_e32 v53, v101
	ds_read_b128 v[190:193], v3 offset:6144
	ds_read_b128 v[170:173], v3 offset:6656
	v_mfma_f32_32x32x16_bf16 v[34:49], v[178:181], v[12:15], v[34:49]
	v_exp_f32_e32 v54, v102
	v_exp_f32_e32 v55, v103
	v_exp_f32_e32 v56, v104
	v_exp_f32_e32 v57, v105
	ds_read_b128 v[178:181], v3 offset:8192
	ds_read_b128 v[166:169], v3 offset:8704
	v_mfma_f32_32x32x16_bf16 v[18:33], v[218:221], v[8:11], v[18:33]
	v_exp_f32_e32 v58, v106
	v_exp_f32_e32 v59, v107
	v_exp_f32_e32 v60, v108
	v_exp_f32_e32 v61, v109
	ds_read_b128 v[174:177], v3 offset:10240
	ds_read_b128 v[162:165], v3 offset:10752
	v_mfma_f32_32x32x16_bf16 v[34:49], v[218:221], v[4:7], v[34:49]
	v_exp_f32_e32 v62, v110
	v_exp_f32_e32 v63, v111
	v_exp_f32_e32 v64, v112
	v_exp_f32_e32 v65, v113
	s_mov_b32 s26, s27
	s_cmp_eq_u32 s27, s96
	s_cbranch_scc1 .Lmla_ss1_xdone
	s_add_i32 s64, s27, 3
	s_cmp_lt_u32 s64, s94
	s_cbranch_scc1 .Lmla_ss1_top
	s_waitcnt vmcnt(4)
	s_barrier
	s_branch .Lmla_ss_back
